# best2 + counted waits in out-projection epilogue: the vmcnt(0) drain after the first 16 x-tile loads replaced by per-consumer vmcnt(11/12/16/20)
# baseline (speedup 1.0000x reference)
; #define EPS_LOAD(g_) do { const size_t off_ = (size_t)(row0 + ((g_) >> 2) * HALF + ((g_) & 3) * 16) * ldc + col0; \
;             _Pragma("unroll") for (int bj = 0; bj < 2; ++bj) _Pragma("unroll") for (int n = 0; n < 2; ++n) rb[(g_) & 3][2 * bj + n] = *(const f32x4*)(base + off_ + bj * HALF + n * 16); } while (0)
;     DI void operator()(const f32x4 (&acc)[2][2][4][2], const Unit& u, int wr, int wc, int fr, int fq, const LAS unsigned char* st) const {
;         const int row0 = u.pm * BM + wr * 64 + fr, col0 = u.pn * BM + wc * 32 + 4 * fq;
;         f32x4 rb[4][4];
;     ...
;         EPS_LOAD(0); EPS_LOAD(1); EPS_LOAD(2);
; #pragma unroll
;         for (int ai = 0; ai < 2; ++ai)
; #pragma unroll
;             for (int m = 0; m < 4; ++m) { const int g = 4 * ai + m; const size_t off = (size_t)(row0 + ai * HALF + m * 16) * ldc + col0;
;                 if (g + 3 < 8) EPS_LOAD(g + 3);
; #pragma unroll
;                 for (int bj = 0; bj < 2; ++bj)
; #pragma unroll
;                     for (int n = 0; n < 2; ++n) *(f32x4*)(C + off + bj * HALF + n * 16) = rb[g & 3][2 * bj + n] + acc[ai][bj][m][n]; }
.LBB0_796:
	v_mov_b32_e32 v130, v224
	s_lshl_b32 s0, s28, 8
	s_add_i32 s0, s0, s45
	v_and_or_b32 v140, v130, 15, s0
	s_lshl_b32 s0, s54, 8
	v_ashrrev_i32_e32 v130, 2, v130
	s_or_b32 s0, s0, s46
	v_and_b32_e32 v130, -4, v130
	v_add_u32_e32 v136, s0, v130
	v_ashrrev_i32_e32 v141, 31, v140
	v_readlane_b32 s0, v254, 3
	v_or_b32_e32 v168, 16, v140
	v_or_b32_e32 v184, 32, v140
	v_ashrrev_i32_e32 v137, 31, v136
	v_lshlrev_b64 v[138:139], 13, v[140:141]
	v_readlane_b32 s1, v254, 4
	v_ashrrev_i32_e32 v169, 31, v168
	v_ashrrev_i32_e32 v185, 31, v184
	v_lshl_add_u64 v[152:153], s[0:1], 0, v[138:139]
	v_lshlrev_b64 v[136:137], 2, v[136:137]
	v_lshlrev_b64 v[216:217], 13, v[168:169]
	v_lshlrev_b64 v[218:219], 13, v[184:185]
	v_lshl_add_u64 v[164:165], v[152:153], 0, v[136:137]
	v_lshl_add_u64 v[168:169], s[0:1], 0, v[216:217]
	v_lshl_add_u64 v[184:185], s[0:1], 0, v[218:219]
	global_load_dwordx4 v[152:155], v[164:165], off
	global_load_dwordx4 v[156:159], v[164:165], off offset:64
	global_load_dwordx4 v[160:163], v[164:165], off offset:512
	s_nop 0
	global_load_dwordx4 v[164:167], v[164:165], off offset:576
	v_lshl_add_u64 v[180:181], v[168:169], 0, v[136:137]
	v_lshl_add_u64 v[196:197], v[184:185], 0, v[136:137]
	global_load_dwordx4 v[168:171], v[180:181], off
	global_load_dwordx4 v[172:175], v[180:181], off offset:64
	global_load_dwordx4 v[176:179], v[180:181], off offset:512
	s_nop 0
	global_load_dwordx4 v[180:183], v[180:181], off offset:576
	s_nop 0
	global_load_dwordx4 v[184:187], v[196:197], off
	global_load_dwordx4 v[188:191], v[196:197], off offset:64
	global_load_dwordx4 v[192:195], v[196:197], off offset:512
	s_nop 0
	global_load_dwordx4 v[196:199], v[196:197], off offset:576
	v_or_b32_e32 v200, 48, v140
	v_ashrrev_i32_e32 v201, 31, v200
	v_lshlrev_b64 v[220:221], 13, v[200:201]
	v_lshl_add_u64 v[200:201], s[0:1], 0, v[220:221]
	v_lshl_add_u64 v[212:213], v[200:201], 0, v[136:137]
	global_load_dwordx4 v[200:203], v[212:213], off
	global_load_dwordx4 v[204:207], v[212:213], off offset:64
	global_load_dwordx4 v[208:211], v[212:213], off offset:512
	s_nop 0
	global_load_dwordx4 v[212:215], v[212:213], off offset:576
	v_lshl_add_u64 v[222:223], s[92:93], 0, v[138:139]
	v_lshl_add_u64 v[226:227], v[138:139], 0, s[74:75]
	v_lshl_add_u64 v[228:229], v[138:139], 0, s[76:77]
	v_lshl_add_u64 v[230:231], s[0:1], 0, v[226:227]
	v_lshl_add_u64 v[216:217], s[92:93], 0, v[216:217]
	v_lshl_add_u64 v[138:139], v[222:223], 0, v[136:137]
	v_lshl_add_u64 v[232:233], s[0:1], 0, v[228:229]
	v_lshl_add_u64 v[218:219], s[92:93], 0, v[218:219]
	v_lshl_add_u64 v[222:223], v[230:231], 0, v[136:137]
	v_lshl_add_u64 v[216:217], v[216:217], 0, v[136:137]
	v_lshl_add_u64 v[230:231], v[232:233], 0, v[136:137]
	v_readlane_b32 s2, v254, 5
	v_readlane_b32 s3, v254, 6
	v_readlane_b32 s4, v254, 7
	v_readlane_b32 s5, v254, 8
	v_readlane_b32 s6, v254, 9
	v_readlane_b32 s7, v254, 10
	v_readlane_b32 s8, v254, 11
	v_readlane_b32 s9, v254, 12
	v_readlane_b32 s10, v254, 13
	v_readlane_b32 s11, v254, 14
	v_readlane_b32 s12, v254, 15
	v_readlane_b32 s13, v254, 16
	v_readlane_b32 s14, v254, 17
	v_readlane_b32 s15, v254, 18
	s_waitcnt vmcnt(11)
	v_pk_add_f32 v[128:129], v[128:129], v[154:155]
	v_pk_add_f32 v[126:127], v[126:127], v[152:153]
	v_pk_add_f32 v[124:125], v[124:125], v[158:159]
	v_pk_add_f32 v[122:123], v[122:123], v[156:157]
	v_pk_add_f32 v[108:109], v[108:109], v[162:163]
	v_pk_add_f32 v[106:107], v[106:107], v[160:161]
	v_pk_add_f32 v[104:105], v[104:105], v[166:167]
	v_pk_add_f32 v[102:103], v[102:103], v[164:165]
	v_pk_add_f32 v[120:121], v[120:121], v[170:171]
	v_pk_add_f32 v[118:119], v[118:119], v[168:169]
	global_store_dwordx4 v[138:139], v[126:129], off
	global_store_dwordx4 v[138:139], v[122:125], off offset:64
	global_store_dwordx4 v[138:139], v[106:109], off offset:512
	global_store_dwordx4 v[138:139], v[102:105], off offset:576
	s_waitcnt vmcnt(12)
	v_pk_add_f32 v[116:117], v[116:117], v[174:175]
	v_pk_add_f32 v[114:115], v[114:115], v[172:173]
	v_pk_add_f32 v[100:101], v[100:101], v[178:179]
	v_pk_add_f32 v[98:99], v[98:99], v[176:177]
	v_pk_add_f32 v[96:97], v[96:97], v[182:183]
	v_pk_add_f32 v[94:95], v[94:95], v[180:181]
	global_load_dwordx4 v[102:105], v[222:223], off
	global_load_dwordx4 v[106:109], v[222:223], off offset:64
	global_load_dwordx4 v[122:125], v[222:223], off offset:512
	global_load_dwordx4 v[126:129], v[222:223], off offset:576
	s_nop 0
	global_store_dwordx4 v[216:217], v[118:121], off
	global_store_dwordx4 v[216:217], v[114:117], off offset:64
	global_store_dwordx4 v[216:217], v[98:101], off offset:512
	global_store_dwordx4 v[216:217], v[94:97], off offset:576
	v_lshl_add_u64 v[152:153], v[218:219], 0, v[136:137]
	s_waitcnt vmcnt(16)
; #define EPS_LOAD(g_) do { const size_t off_ = (size_t)(row0 + ((g_) >> 2) * HALF + ((g_) & 3) * 16) * ldc + col0; \
;             _Pragma("unroll") for (int bj = 0; bj < 2; ++bj) _Pragma("unroll") for (int n = 0; n < 2; ++n) rb[(g_) & 3][2 * bj + n] = *(const f32x4*)(base + off_ + bj * HALF + n * 16); } while (0)
;     DI void operator()(const f32x4 (&acc)[2][2][4][2], const Unit& u, int wr, int wc, int fr, int fq, const LAS unsigned char* st) const {
;         const int row0 = u.pm * BM + wr * 64 + fr, col0 = u.pn * BM + wc * 32 + 4 * fq;
;         f32x4 rb[4][4];
;     ...
;         EPS_LOAD(0); EPS_LOAD(1); EPS_LOAD(2);
; #pragma unroll
;         for (int ai = 0; ai < 2; ++ai)
; #pragma unroll
;             for (int m = 0; m < 4; ++m) { const int g = 4 * ai + m; const size_t off = (size_t)(row0 + ai * HALF + m * 16) * ldc + col0;
;                 if (g + 3 < 8) EPS_LOAD(g + 3);
; #pragma unroll
;                 for (int bj = 0; bj < 2; ++bj)
; #pragma unroll
;                     for (int n = 0; n < 2; ++n) *(f32x4*)(C + off + bj * HALF + n * 16) = rb[g & 3][2 * bj + n] + acc[ai][bj][m][n]; }
	v_pk_add_f32 v[80:81], v[80:81], v[198:199]
	v_pk_add_f32 v[78:79], v[78:79], v[196:197]
	global_load_dwordx4 v[94:97], v[230:231], off
	global_load_dwordx4 v[98:101], v[230:231], off offset:64
	global_load_dwordx4 v[114:117], v[230:231], off offset:512
	global_load_dwordx4 v[118:121], v[230:231], off offset:576
	v_pk_add_f32 v[112:113], v[112:113], v[186:187]
	global_store_dwordx4 v[152:153], v[78:81], off offset:576
	v_pk_add_f32 v[110:111], v[110:111], v[184:185]
	v_pk_add_f32 v[92:93], v[92:93], v[190:191]
	v_add_u32_e32 v78, 0xa0, v140
	v_ashrrev_i32_e32 v79, 31, v78
	v_pk_add_f32 v[90:91], v[90:91], v[188:189]
	v_pk_add_f32 v[88:89], v[88:89], v[194:195]
	v_pk_add_f32 v[86:87], v[86:87], v[192:193]
	v_lshlrev_b64 v[78:79], 13, v[78:79]
	global_store_dwordx4 v[152:153], v[110:113], off
	global_store_dwordx4 v[152:153], v[90:93], off offset:64
	global_store_dwordx4 v[152:153], v[86:89], off offset:512
	v_lshl_add_u64 v[78:79], s[0:1], 0, v[78:79]
	v_lshl_add_u64 v[152:153], s[92:93], 0, v[220:221]
	v_lshl_add_u64 v[110:111], v[78:79], 0, v[136:137]
	v_lshl_add_u64 v[152:153], v[152:153], 0, v[136:137]
	s_waitcnt vmcnt(20)
	v_pk_add_f32 v[68:69], v[68:69], v[214:215]
	v_pk_add_f32 v[66:67], v[66:67], v[212:213]
	global_load_dwordx4 v[78:81], v[110:111], off
	global_load_dwordx4 v[86:89], v[110:111], off offset:64
	global_load_dwordx4 v[90:93], v[110:111], off offset:512
	s_nop 0
	global_load_dwordx4 v[110:113], v[110:111], off offset:576
	v_pk_add_f32 v[84:85], v[84:85], v[202:203]
	global_store_dwordx4 v[152:153], v[66:69], off offset:576
	v_pk_add_f32 v[82:83], v[82:83], v[200:201]
	v_pk_add_f32 v[76:77], v[76:77], v[206:207]
	v_add_u32_e32 v66, 0xb0, v140
	v_ashrrev_i32_e32 v67, 31, v66
	v_lshlrev_b64 v[66:67], 13, v[66:67]
	v_pk_add_f32 v[74:75], v[74:75], v[204:205]
	v_pk_add_f32 v[72:73], v[72:73], v[210:211]
	v_pk_add_f32 v[70:71], v[70:71], v[208:209]
	v_lshl_add_u64 v[66:67], s[0:1], 0, v[66:67]
	global_store_dwordx4 v[152:153], v[82:85], off
	global_store_dwordx4 v[152:153], v[74:77], off offset:64
	global_store_dwordx4 v[152:153], v[70:73], off offset:512
	v_lshl_add_u64 v[82:83], v[66:67], 0, v[136:137]
	global_load_dwordx4 v[66:69], v[82:83], off
	global_load_dwordx4 v[70:73], v[82:83], off offset:64
	global_load_dwordx4 v[74:77], v[82:83], off offset:512
	s_nop 0
	global_load_dwordx4 v[82:85], v[82:83], off offset:576
	v_lshl_add_u64 v[140:141], s[92:93], 0, v[226:227]
	v_lshl_add_u64 v[152:153], s[92:93], 0, v[228:229]
	v_lshl_add_u64 v[140:141], v[140:141], 0, v[136:137]
	v_lshl_add_u64 v[136:137], v[152:153], 0, v[136:137]
	v_add_co_u32_e32 v154, vcc, s52, v138
	v_lshl_add_u64 v[152:153], v[138:139], 0, s[16:17]
	s_nop 0
	v_addc_co_u32_e32 v155, vcc, 0, v139, vcc
	s_mov_b64 s[0:1], -1
	s_waitcnt vmcnt(27)
	v_pk_add_f32 v[64:65], v[64:65], v[104:105]
	v_pk_add_f32 v[62:63], v[62:63], v[102:103]
	s_waitcnt vmcnt(26)
	v_pk_add_f32 v[60:61], v[60:61], v[108:109]
	s_waitcnt vmcnt(24)
	v_pk_add_f32 v[40:41], v[40:41], v[128:129]
	v_pk_add_f32 v[38:39], v[38:39], v[126:127]
	v_pk_add_f32 v[58:59], v[58:59], v[106:107]
	v_pk_add_f32 v[48:49], v[48:49], v[124:125]
	v_pk_add_f32 v[46:47], v[46:47], v[122:123]
	global_store_dwordx4 v[140:141], v[62:65], off
	global_store_dwordx4 v[140:141], v[58:61], off offset:64
	global_store_dwordx4 v[140:141], v[46:49], off offset:512
	global_store_dwordx4 v[140:141], v[38:41], off offset:576
	s_waitcnt vmcnt(20)
	v_pk_add_f32 v[28:29], v[28:29], v[120:121]
	v_pk_add_f32 v[26:27], v[26:27], v[118:119]
	v_pk_add_f32 v[40:41], v[56:57], v[96:97]
	v_pk_add_f32 v[38:39], v[54:55], v[94:95]
	v_pk_add_f32 v[48:49], v[52:53], v[100:101]
	v_pk_add_f32 v[46:47], v[50:51], v[98:99]
	v_pk_add_f32 v[32:33], v[32:33], v[116:117]
	v_pk_add_f32 v[30:31], v[30:31], v[114:115]
	global_store_dwordx4 v[136:137], v[38:41], off
	global_store_dwordx4 v[136:137], v[46:49], off offset:64
	global_store_dwordx4 v[136:137], v[30:33], off offset:512
	global_store_dwordx4 v[136:137], v[26:29], off offset:576
	s_waitcnt vmcnt(17)
	v_pk_add_f32 v[20:21], v[20:21], v[92:93]
	v_pk_add_f32 v[28:29], v[44:45], v[80:81]
	v_pk_add_f32 v[26:27], v[42:43], v[78:79]
	v_pk_add_f32 v[18:19], v[18:19], v[90:91]
	v_pk_add_f32 v[32:33], v[36:37], v[88:89]
	v_pk_add_f32 v[30:31], v[34:35], v[86:87]
	global_store_dwordx4 v[154:155], v[26:29], off
	global_store_dwordx4 v[152:153], v[30:33], off offset:64
	global_store_dwordx4 v[152:153], v[18:21], off offset:512
	s_waitcnt vmcnt(19)
	v_pk_add_f32 v[16:17], v[16:17], v[112:113]
	v_pk_add_f32 v[14:15], v[14:15], v[110:111]
	v_add_co_u32_e32 v20, vcc, s53, v138
	global_store_dwordx4 v[152:153], v[14:17], off offset:576
	s_nop 0
	v_addc_co_u32_e32 v21, vcc, 0, v139, vcc
	s_waitcnt vmcnt(15)
	v_pk_add_f32 v[16:17], v[24:25], v[68:69]
	v_pk_add_f32 v[14:15], v[22:23], v[66:67]
	v_lshl_add_u64 v[18:19], v[138:139], 0, s[18:19]
	s_waitcnt vmcnt(14)
	v_pk_add_f32 v[12:13], v[12:13], v[72:73]
	v_pk_add_f32 v[10:11], v[10:11], v[70:71]
	s_waitcnt vmcnt(13)
	v_pk_add_f32 v[8:9], v[8:9], v[76:77]
	v_pk_add_f32 v[6:7], v[6:7], v[74:75]
	s_waitcnt vmcnt(12)
	v_pk_add_f32 v[4:5], v[4:5], v[84:85]
	v_pk_add_f32 v[2:3], v[2:3], v[82:83]
	s_andn2_b64 vcc, exec, s[60:61]
	global_store_dwordx4 v[20:21], v[14:17], off
	global_store_dwordx4 v[18:19], v[10:13], off offset:64
	global_store_dwordx4 v[18:19], v[6:9], off offset:512
	global_store_dwordx4 v[18:19], v[2:5], off offset:576
	s_cbranch_vccnz .LBB0_785
	s_andn2_b64 vcc, exec, s[64:65]
	s_cbranch_vccnz .LBB0_784
	s_barrier
	s_branch .LBB0_784
